# phase-3 RG-LRU output unit: second direction's nine aggregate loads issued together with the first direction's (one dependent round trip less per unit)
# speedup vs baseline: 1.0074x; 1.0004x over previous
; __device__ __forceinline__ void lru_out_unit(const Args& a, unsigned char* lds_g, int b, int cidx, int blk, int tid, unsigned (&psw)[2][16], int nb, int ncidx, int nblk) {
;     ...
;     for (int d = 0; d < 2; ++d)
; #pragma unroll
;         for (int i = 0; i < 16; ++i) { const unsigned wv = psw[d][i]; av[d][i] = 1.f - bflo(wv); bv[d][i] = bfhi(wv); }
;     const int p0 = (cidx - 4) * 64 + 16 * q;
;     unsigned short ugv[16];
; #pragma unroll
;     for (int i = 0; i < 16; ++i) ugv[i] = ((const bf16*)(a.ws + WS_UG))[(size_t)(lru_pos_row(b, false, p0 + i) - NCTX) * 1024 + ch];
;     if (ncidx >= 0) lru_out_loadps(a, nb, ncidx, nblk, tid, psw);
;     float2* CA = (float2*)(lds_g + 8192);
; #pragma unroll
;     for (int d = 0; d < 2; ++d) { const float2* AGG = (const float2*)(a.ws + WS_AGG) + ((size_t)(b * 2 + d) * 36) * 1024 + ch; float2 qv[9];
; #pragma unroll
;         for (int i = 0; i < 9; ++i) { const int sidx = 9 * q + i; const int c2 = d ? (sidx < 4 ? 3 - sidx : 39 - sidx) : sidx; qv[i] = AGG[(size_t)c2 * 1024]; }
.LBB0_672:
	v_lshlrev_b32_e32 v66, 16, v32
	v_and_b32_e32 v125, 0xffff0000, v32
	v_lshlrev_b32_e32 v32, 16, v33
	v_sub_f32_e32 v126, 1.0, v32
	v_lshlrev_b32_e32 v32, 16, v35
	v_sub_f32_e32 v131, 1.0, v66
	v_sub_f32_e32 v66, 1.0, v32
	v_lshlrev_b32_e32 v32, 16, v36
	v_sub_f32_e32 v72, 1.0, v32
	v_lshlrev_b32_e32 v32, 16, v37
	v_sub_f32_e32 v68, 1.0, v32
	v_lshlrev_b32_e32 v32, 16, v39
	v_and_b32_e32 v117, 0xffff0000, v33
	v_sub_f32_e32 v70, 1.0, v32
	v_lshlrev_b32_e32 v33, 16, v41
	v_lshlrev_b32_e32 v32, 16, v34
	v_pk_add_f32 v[74:75], v[32:33], 1.0 op_sel_hi:[1,0] neg_lo:[1,0] neg_hi:[1,0]
	v_lshlrev_b32_e32 v33, 16, v43
	v_lshlrev_b32_e32 v32, 16, v38
	v_pk_add_f32 v[76:77], v[32:33], 1.0 op_sel_hi:[1,0] neg_lo:[1,0] neg_hi:[1,0]
	v_lshlrev_b32_e32 v32, 16, v40
	v_lshlrev_b32_e32 v33, 16, v44
	v_and_b32_e32 v118, 0xffff0000, v34
	v_and_b32_e32 v120, 0xffff0000, v36
	v_and_b32_e32 v121, 0xffff0000, v37
	v_lshlrev_b32_e32 v37, 16, v45
	v_lshlrev_b32_e32 v36, 16, v42
	v_mov_b32_e32 v34, v33
	v_pk_add_f32 v[92:93], v[32:33], 1.0 op_sel_hi:[1,0] neg_lo:[1,0] neg_hi:[1,0]
	v_lshlrev_b32_e32 v32, 16, v48
	v_lshlrev_b32_e32 v33, 16, v49
	v_pk_add_f32 v[88:89], v[36:37], 1.0 op_sel_hi:[1,0] neg_lo:[1,0] neg_hi:[1,0]
	v_and_b32_e32 v95, 0xffff0000, v48
	v_and_b32_e32 v128, 0xffff0000, v49
	v_mov_b32_e32 v37, v33
	v_pk_add_f32 v[48:49], v[32:33], 1.0 op_sel_hi:[1,0] neg_lo:[1,0] neg_hi:[1,0]
	v_lshlrev_b32_e32 v33, 16, v50
	v_lshlrev_b32_e32 v32, 16, v53
	v_and_b32_e32 v123, 0xffff0000, v39
	v_and_b32_e32 v71, 0xffff0000, v43
	v_and_b32_e32 v43, 0xffff0000, v45
	v_lshlrev_b32_e32 v39, 16, v47
	v_and_b32_e32 v87, 0xffff0000, v47
	v_and_b32_e32 v45, 0xffff0000, v50
	v_and_b32_e32 v47, 0xffff0000, v51
	v_lshlrev_b32_e32 v36, 16, v51
	v_pk_add_f32 v[50:51], v[32:33], 1.0 op_sel_hi:[1,0] neg_lo:[1,0] neg_hi:[1,0]
	v_lshlrev_b32_e32 v32, 16, v56
	v_sub_f32_e32 v78, 1.0, v32
	v_lshlrev_b32_e32 v33, 16, v52
	v_lshlrev_b32_e32 v32, 16, v57
	v_and_b32_e32 v79, 0xffff0000, v52
	v_and_b32_e32 v81, 0xffff0000, v53
	v_pk_add_f32 v[52:53], v[32:33], 1.0 op_sel_hi:[1,0] neg_lo:[1,0] neg_hi:[1,0]
	v_lshlrev_b32_e32 v32, 16, v58
	v_sub_f32_e32 v80, 1.0, v32
	v_lshlrev_b32_e32 v32, 16, v59
	v_and_b32_e32 v130, 0xffff0000, v56
	v_sub_f32_e32 v56, 1.0, v32
	v_lshlrev_b32_e32 v32, 16, v60
	s_and_b32 s55, s57, 0x1fffff80
	v_and_b32_e32 v119, 0xffff0000, v35
	v_lshlrev_b32_e32 v35, 16, v46
	v_sub_f32_e32 v82, 1.0, v32
	v_lshlrev_b32_e32 v33, 16, v54
	v_lshlrev_b32_e32 v32, 16, v61
	s_lshl_b32 s55, s55, 3
	v_and_b32_e32 v122, 0xffff0000, v38
	v_mov_b32_e32 v38, v35
	v_pk_add_f32 v[90:91], v[34:35], 1.0 op_sel_hi:[1,0] neg_lo:[1,0] neg_hi:[1,0]
	v_and_b32_e32 v83, 0xffff0000, v54
	v_lshlrev_b32_e32 v34, 16, v55
	v_mov_b32_e32 v35, v36
	v_pk_add_f32 v[96:97], v[36:37], 1.0 op_sel_hi:[1,0] neg_lo:[1,0] neg_hi:[1,0]
	v_and_b32_e32 v129, 0xffff0000, v55
	v_pk_add_f32 v[54:55], v[32:33], 1.0 op_sel_hi:[1,0] neg_lo:[1,0] neg_hi:[1,0]
	v_lshlrev_b32_e32 v32, 16, v62
	s_lshl_b32 s77, s56, 1
	s_add_i32 s55, s55, 0
	v_lshlrev_b32_e32 v36, 3, v73
	s_mul_i32 s56, s56, 0x90000
	v_sub_f32_e32 v133, 1.0, v32
	v_lshlrev_b32_e32 v32, 16, v63
	s_mul_i32 s54, s75, 9
	v_add_u32_e32 v37, s55, v36
	s_mul_hi_i32 s55, s77, 0x48000
	s_add_u32 s56, s1, s56
	v_sub_f32_e32 v134, 1.0, v32
	s_addc_u32 s57, s2, s55
	v_lshlrev_b64 v[32:33], 3, v[64:65]
	s_ashr_i32 s55, s54, 31
	v_pk_add_f32 v[98:99], v[34:35], 1.0 op_sel_hi:[1,0] neg_lo:[1,0] neg_hi:[1,0]
	v_lshl_add_u64 v[34:35], s[56:57], 0, v[32:33]
	s_lshl_b64 s[56:57], s[54:55], 13
	s_add_i32 s64, s54, 1
	v_pk_add_f32 v[84:85], v[38:39], 1.0 op_sel_hi:[1,0] neg_lo:[1,0] neg_hi:[1,0]
	v_lshl_add_u64 v[38:39], v[34:35], 0, s[56:57]
	s_ashr_i32 s65, s64, 31
	global_load_dwordx2 v[38:39], v[38:39], off
	s_lshl_b64 s[56:57], s[64:65], 13
	s_add_i32 s68, s54, 2
	v_lshl_add_u64 v[136:137], v[34:35], 0, s[56:57]
	s_ashr_i32 s69, s68, 31
	global_load_dwordx2 v[136:137], v[136:137], off
	s_lshl_b64 s[56:57], s[68:69], 13
	s_add_i32 s66, s54, 3
	v_lshl_add_u64 v[138:139], v[34:35], 0, s[56:57]
	s_ashr_i32 s67, s66, 31
	global_load_dwordx2 v[138:139], v[138:139], off
	s_lshl_b64 s[56:57], s[66:67], 13
	s_add_i32 s62, s54, 4
	v_lshl_add_u64 v[140:141], v[34:35], 0, s[56:57]
	s_ashr_i32 s63, s62, 31
	global_load_dwordx2 v[140:141], v[140:141], off
	s_lshl_b64 s[56:57], s[62:63], 13
	s_add_i32 s60, s54, 5
	v_lshl_add_u64 v[142:143], v[34:35], 0, s[56:57]
	s_ashr_i32 s61, s60, 31
	s_add_i32 s58, s54, 6
	global_load_dwordx2 v[142:143], v[142:143], off
	s_lshl_b64 s[56:57], s[60:61], 13
	s_ashr_i32 s59, s58, 31
	v_lshl_add_u64 v[144:145], v[34:35], 0, s[56:57]
	s_lshl_b64 s[56:57], s[58:59], 13
	global_load_dwordx2 v[144:145], v[144:145], off
	v_lshl_add_u64 v[146:147], v[34:35], 0, s[56:57]
	s_add_i32 s56, s54, 7
	s_ashr_i32 s57, s56, 31
	global_load_dwordx2 v[146:147], v[146:147], off
	s_lshl_b64 s[70:71], s[56:57], 13
	v_lshl_add_u64 v[148:149], v[34:35], 0, s[70:71]
	global_load_dwordx2 v[148:149], v[148:149], off
	s_add_i32 s70, s54, 8
	s_ashr_i32 s71, s70, 31
	s_lshl_b64 s[80:81], s[70:71], 13
	v_lshl_add_u64 v[34:35], v[34:35], 0, s[80:81]
	global_load_dwordx2 v[34:35], v[34:35], off
	s_or_b32 s92, s77, 1
	s_mul_hi_i32 s89, s92, 0x48000
	s_mul_i32 s88, s92, 0x48000
	s_add_u32 s88, s1, s88
	s_addc_u32 s89, s2, s89
	v_lshl_add_u64 v[168:169], s[88:89], 0, v[32:33]
	s_cmp_gt_i32 s75, 0
	s_cselect_b32 s90, 39, 3
	s_cmp_gt_i32 s75, -1
	s_cselect_b32 s91, 39, 3
	s_sub_i32 s94, s90, s54
	s_ashr_i32 s95, s94, 31
	s_lshl_b64 s[94:95], s[94:95], 13
	v_lshl_add_u64 v[150:151], v[168:169], 0, s[94:95]
	global_load_dwordx2 v[150:151], v[150:151], off
	s_sub_i32 s94, s90, s54
; __device__ __forceinline__ void lru_out_unit(const Args& a, unsigned char* lds_g, int b, int cidx, int blk, int tid, unsigned (&psw)[2][16], int nb, int ncidx, int nblk) {
;     ...
;     for (int d = 0; d < 2; ++d) { const float2* AGG = (const float2*)(a.ws + WS_AGG) + ((size_t)(b * 2 + d) * 36) * 1024 + ch; float2 qv[9];
; #pragma unroll
;         for (int i = 0; i < 9; ++i) { const int sidx = 9 * q + i; const int c2 = d ? (sidx < 4 ? 3 - sidx : 39 - sidx) : sidx; qv[i] = AGG[(size_t)c2 * 1024]; }
;         float P = 1.f, S = 0.f;
; #pragma unroll
;         for (int i = 0; i < 9; ++i) { const int sidx = 9 * q + i; const int c2 = d ? (sidx < 4 ? 3 - sidx : 39 - sidx) : sidx; const bool use = d ? (sidx < 4 || c2 > cidx) : (c2 < cidx);
;             S = use ? qv[i].x * S + qv[i].y : S; P = use ? qv[i].x * P : P; }
	s_sub_i32 s94, s94, 1
	s_ashr_i32 s95, s94, 31
	s_lshl_b64 s[94:95], s[94:95], 13
	v_lshl_add_u64 v[152:153], v[168:169], 0, s[94:95]
	global_load_dwordx2 v[152:153], v[152:153], off
	s_sub_i32 s94, s90, s54
	s_sub_i32 s94, s94, 2
	s_ashr_i32 s95, s94, 31
	s_lshl_b64 s[94:95], s[94:95], 13
	v_lshl_add_u64 v[154:155], v[168:169], 0, s[94:95]
	global_load_dwordx2 v[154:155], v[154:155], off
	s_sub_i32 s94, s90, s54
	s_sub_i32 s94, s94, 3
	s_ashr_i32 s95, s94, 31
	s_lshl_b64 s[94:95], s[94:95], 13
	v_lshl_add_u64 v[156:157], v[168:169], 0, s[94:95]
	global_load_dwordx2 v[156:157], v[156:157], off
	s_sub_i32 s94, s91, s54
	s_sub_i32 s94, s94, 4
	s_ashr_i32 s95, s94, 31
	s_lshl_b64 s[94:95], s[94:95], 13
	v_lshl_add_u64 v[158:159], v[168:169], 0, s[94:95]
	global_load_dwordx2 v[158:159], v[158:159], off
	s_sub_i32 s94, s91, s54
	s_sub_i32 s94, s94, 5
	s_ashr_i32 s95, s94, 31
	s_lshl_b64 s[94:95], s[94:95], 13
	v_lshl_add_u64 v[160:161], v[168:169], 0, s[94:95]
	global_load_dwordx2 v[160:161], v[160:161], off
	s_sub_i32 s94, s91, s54
	s_sub_i32 s94, s94, 6
	s_ashr_i32 s95, s94, 31
	s_lshl_b64 s[94:95], s[94:95], 13
	v_lshl_add_u64 v[162:163], v[168:169], 0, s[94:95]
	global_load_dwordx2 v[162:163], v[162:163], off
	s_sub_i32 s94, s91, s54
	s_sub_i32 s94, s94, 7
	s_ashr_i32 s95, s94, 31
	s_lshl_b64 s[94:95], s[94:95], 13
	v_lshl_add_u64 v[164:165], v[168:169], 0, s[94:95]
	global_load_dwordx2 v[164:165], v[164:165], off
	s_sub_i32 s94, s91, s54
	s_sub_i32 s94, s94, 8
	s_ashr_i32 s95, s94, 31
	s_lshl_b64 s[94:95], s[94:95], 13
	v_lshl_add_u64 v[166:167], v[168:169], 0, s[94:95]
	global_load_dwordx2 v[166:167], v[166:167], off
	s_cmp_lt_i32 s54, s78
	s_cselect_b64 vcc, -1, 0
	s_cmp_lt_i32 s64, s78
	v_and_b32_e32 v124, 0xffff0000, v40
	v_and_b32_e32 v67, 0xffff0000, v41
	v_and_b32_e32 v69, 0xffff0000, v42
	v_and_b32_e32 v41, 0xffff0000, v44
	v_mov_b32_e32 v42, v77
	v_and_b32_e32 v127, 0xffff0000, v46
	v_mov_b32_e32 v86, v85
	v_and_b32_e32 v63, 0xffff0000, v63
	v_and_b32_e32 v62, 0xffff0000, v62
	v_and_b32_e32 v61, 0xffff0000, v61
	v_and_b32_e32 v60, 0xffff0000, v60
	v_and_b32_e32 v59, 0xffff0000, v59
	v_and_b32_e32 v58, 0xffff0000, v58
	v_and_b32_e32 v132, 0xffff0000, v57
	v_mov_b32_e32 v46, v55
	v_mov_b32_e32 v44, v53
	v_mov_b32_e32 v94, v48
	s_waitcnt vmcnt(17)
	v_fma_f32 v39, 0, v38, v39
	v_cndmask_b32_e32 v39, 0, v39, vcc
	v_cndmask_b32_e32 v38, 1.0, v38, vcc
	s_cselect_b64 vcc, -1, 0
	s_cmp_lt_i32 s68, s78
	s_waitcnt vmcnt(16)
	v_fma_f32 v40, v136, v39, v137
	v_cndmask_b32_e32 v39, v39, v40, vcc
	v_mul_f32_e32 v40, v38, v136
	v_cndmask_b32_e32 v38, v38, v40, vcc
	s_cselect_b64 vcc, -1, 0
	s_waitcnt vmcnt(15)
	v_fma_f32 v40, v138, v39, v139
	v_cndmask_b32_e32 v39, v39, v40, vcc
	v_mul_f32_e32 v40, v38, v138
	s_cmp_lt_i32 s66, s78
	v_cndmask_b32_e32 v38, v38, v40, vcc
	s_cselect_b64 vcc, -1, 0
	s_waitcnt vmcnt(14)
	v_fma_f32 v40, v140, v39, v141
	v_cndmask_b32_e32 v39, v39, v40, vcc
	v_mul_f32_e32 v40, v38, v140
	s_cmp_lt_i32 s54, s76
	v_cndmask_b32_e32 v38, v38, v40, vcc
	s_cselect_b64 vcc, -1, 0
	s_waitcnt vmcnt(13)
	v_fma_f32 v40, v142, v39, v143
	v_cndmask_b32_e32 v39, v39, v40, vcc
	v_mul_f32_e32 v40, v38, v142
	s_cmp_lt_i32 s60, s78
	v_cndmask_b32_e32 v38, v38, v40, vcc
	s_cselect_b64 vcc, -1, 0
	s_waitcnt vmcnt(12)
	v_fma_f32 v40, v144, v39, v145
	v_cndmask_b32_e32 v39, v39, v40, vcc
	v_mul_f32_e32 v40, v38, v144
	s_cmp_lt_i32 s58, s78
	v_cndmask_b32_e32 v38, v38, v40, vcc
	s_cselect_b64 vcc, -1, 0
	s_waitcnt vmcnt(11)
	v_fma_f32 v40, v146, v39, v147
	v_cndmask_b32_e32 v39, v39, v40, vcc
	v_mul_f32_e32 v40, v38, v146
	s_cmp_lt_i32 s56, s78
	v_cndmask_b32_e32 v38, v38, v40, vcc
	s_cselect_b64 vcc, -1, 0
	s_waitcnt vmcnt(10)
	v_fma_f32 v40, v148, v39, v149
	v_cndmask_b32_e32 v39, v39, v40, vcc
	v_mul_f32_e32 v40, v38, v148
	s_cmp_lt_i32 s70, s78
	v_cndmask_b32_e32 v38, v38, v40, vcc
	s_cselect_b64 vcc, -1, 0
	s_or_b32 s55, s77, 1
	s_mul_hi_i32 s57, s55, 0x48000
	s_mul_i32 s55, s55, 0x48000
	s_add_u32 s76, s1, s55
	s_addc_u32 s77, s2, s57
	s_cmp_gt_i32 s75, 0
	s_cselect_b32 s57, 39, 3
	s_sub_i32 s76, s57, s54
	s_ashr_i32 s77, s76, 31
	s_waitcnt vmcnt(9)
	v_fma_f32 v35, v34, v39, v35
	v_mul_f32_e32 v34, v38, v34
	s_lshl_b64 s[54:55], s[76:77], 13
	s_sub_i32 s64, s57, s64
	v_cndmask_b32_e32 v35, v39, v35, vcc
	v_cndmask_b32_e32 v34, v38, v34, vcc
	s_ashr_i32 s65, s64, 31
	s_lshl_b64 s[54:55], s[64:65], 13
	s_sub_i32 s68, s57, s68
	s_ashr_i32 s69, s68, 31
	s_lshl_b64 s[54:55], s[68:69], 13
	s_sub_i32 s66, s57, s66
	s_ashr_i32 s67, s66, 31
	s_lshl_b64 s[54:55], s[66:67], 13
	s_cmp_gt_i32 s75, -1
	s_cselect_b32 s65, 39, 3
	s_sub_i32 s62, s65, s62
	s_ashr_i32 s63, s62, 31
	s_lshl_b64 s[54:55], s[62:63], 13
	s_sub_i32 s60, s65, s60
	s_ashr_i32 s61, s60, 31
	s_lshl_b64 s[54:55], s[60:61], 13
	s_sub_i32 s58, s65, s58
	s_ashr_i32 s59, s58, 31
	s_lshl_b64 s[54:55], s[58:59], 13
	s_sub_i32 s56, s65, s56
	s_ashr_i32 s57, s56, 31
	s_lshl_b64 s[54:55], s[56:57], 13
	s_sub_i32 s70, s65, s70
	s_ashr_i32 s71, s70, 31
	s_lshl_b64 s[54:55], s[70:71], 13
	s_cmp_lt_i32 s75, 1
	s_cselect_b64 s[54:55], -1, 0
	s_cmp_gt_i32 s76, s78
	s_cselect_b64 s[76:77], -1, 0
	s_or_b64 vcc, s[54:55], s[76:77]
	s_cmp_gt_i32 s64, s78
	s_cselect_b64 s[64:65], -1, 0
	s_waitcnt vmcnt(8)
	v_fma_f32 v39, 0, v150, v151
	v_cndmask_b32_e32 v39, 0, v39, vcc
	v_cndmask_b32_e32 v38, 1.0, v150, vcc
	s_or_b64 vcc, s[54:55], s[64:65]
	s_waitcnt vmcnt(7)
	v_fma_f32 v40, v152, v39, v153
	s_cmp_gt_i32 s68, s78
	v_cndmask_b32_e32 v39, v39, v40, vcc
	v_mul_f32_e32 v40, v38, v152
	s_cselect_b64 s[64:65], -1, 0
	v_cndmask_b32_e32 v38, v38, v40, vcc
	s_or_b64 vcc, s[54:55], s[64:65]
	s_waitcnt vmcnt(6)
; #define WG_BAR() do { asm volatile("s_waitcnt lgkmcnt(0)" ::: "memory"); __builtin_amdgcn_s_barrier(); asm volatile("" ::: "memory"); } while (0)
; __device__ __forceinline__ void lru_out_unit(const Args& a, unsigned char* lds_g, int b, int cidx, int blk, int tid, unsigned (&psw)[2][16], int nb, int ncidx, int nblk) {
;     ...
;         float P = 1.f, S = 0.f;
; #pragma unroll
;         for (int i = 0; i < 9; ++i) { const int sidx = 9 * q + i; const int c2 = d ? (sidx < 4 ? 3 - sidx : 39 - sidx) : sidx; const bool use = d ? (sidx < 4 || c2 > cidx) : (c2 < cidx);
;             S = use ? qv[i].x * S + qv[i].y : S; P = use ? qv[i].x * P : P; }
;         CA[(d * 4 + q) * 128 + chl] = make_float2(P, S); }
; #pragma unroll
;     for (int d = 0; d < 2; ++d) { float P = 1.f, S = 0.f;
; #pragma unroll
;         for (int ii = 0; ii < 16; ++ii) { const int i = d ? 15 - ii : ii; S = av[d][i] * S + bv[d][i]; P = av[d][i] * P; }
;         QA[(d * 4 + q) * 128 + chl] = make_float2(P, S); }
;     WG_BAR();
;     float hs[16];
; #pragma unroll
;     for (int d = 0; d < 2; ++d) { float h = 0.f;
; #pragma unroll
;         for (int k = 0; k < 4; ++k) { const float2 t = CA[(d * 4 + k) * 128 + chl]; h = t.x * h + t.y; }
; #pragma unroll
;         for (int k = 0; k < 3; ++k) { const int qq = d ? 3 - k : k; const bool use = d ? (qq > q) : (qq < q); const float2 t = QA[(d * 4 + qq) * 128 + chl]; h = use ? t.x * h + t.y : h; }
	v_fma_f32 v40, v154, v39, v155
	s_cmp_gt_i32 s66, s78
	v_cndmask_b32_e32 v39, v39, v40, vcc
	v_mul_f32_e32 v40, v38, v154
	s_cselect_b64 s[64:65], -1, 0
	v_cndmask_b32_e32 v38, v38, v40, vcc
	s_or_b64 vcc, s[54:55], s[64:65]
	s_cmp_lt_i32 s75, 0
	s_waitcnt vmcnt(5)
	v_fma_f32 v40, v156, v39, v157
	s_cselect_b64 s[64:65], -1, 0
	s_cmp_gt_i32 s62, s78
	v_cndmask_b32_e32 v39, v39, v40, vcc
	v_mul_f32_e32 v40, v38, v156
	s_cselect_b64 s[62:63], -1, 0
	v_cndmask_b32_e32 v38, v38, v40, vcc
	s_or_b64 vcc, s[64:65], s[62:63]
	s_waitcnt vmcnt(4)
	v_fma_f32 v40, v158, v39, v159
	s_cmp_gt_i32 s60, s78
	v_cndmask_b32_e32 v39, v39, v40, vcc
	v_mul_f32_e32 v40, v38, v158
	s_cselect_b64 s[60:61], -1, 0
	v_cndmask_b32_e32 v38, v38, v40, vcc
	s_or_b64 vcc, s[64:65], s[60:61]
	s_waitcnt vmcnt(3)
	v_fma_f32 v40, v160, v39, v161
	s_cmp_gt_i32 s58, s78
	v_cndmask_b32_e32 v39, v39, v40, vcc
	v_mul_f32_e32 v40, v38, v160
	s_cselect_b64 s[58:59], -1, 0
	v_cndmask_b32_e32 v38, v38, v40, vcc
	s_or_b64 vcc, s[64:65], s[58:59]
	s_waitcnt vmcnt(2)
	v_fma_f32 v40, v162, v39, v163
	s_cmp_gt_i32 s56, s78
	v_cndmask_b32_e32 v39, v39, v40, vcc
	v_mul_f32_e32 v40, v38, v162
	s_cselect_b64 s[56:57], -1, 0
	v_cndmask_b32_e32 v38, v38, v40, vcc
	s_or_b64 vcc, s[64:65], s[56:57]
	s_waitcnt vmcnt(1)
	v_fma_f32 v40, v164, v39, v165
	v_cndmask_b32_e32 v39, v39, v40, vcc
	v_mul_f32_e32 v40, v38, v164
	s_cmp_gt_i32 s70, s78
	v_cndmask_b32_e32 v38, v38, v40, vcc
	s_cselect_b64 s[56:57], -1, 0
	s_or_b64 vcc, s[64:65], s[56:57]
	s_waitcnt vmcnt(0)
	v_fma_f32 v167, v166, v39, v167
	v_mul_f32_e32 v166, v38, v166
	v_cndmask_b32_e32 v33, v39, v167, vcc
	v_cndmask_b32_e32 v32, v38, v166, vcc
	ds_write2st64_b64 v37, v[34:35], v[32:33] offset0:16 offset1:24
	v_fma_f32 v32, 0, v131, v125
	v_fma_f32 v33, v126, v32, v117
	v_fma_f32 v33, v74, v33, v118
	v_fma_f32 v33, v66, v33, v119
	v_fma_f32 v33, v72, v33, v120
	v_fma_f32 v33, v68, v33, v121
	v_fma_f32 v33, v76, v33, v122
	v_fma_f32 v33, v70, v33, v123
	v_mul_f32_e32 v32, v131, v126
	v_fma_f32 v33, v92, v33, v124
	v_pk_mul_f32 v[34:35], v[74:75], v[32:33]
	v_pk_fma_f32 v[32:33], v[74:75], v[32:33], v[66:67]
	v_pk_mul_f32 v[34:35], v[66:67], v[34:35]
	v_mov_b32_e32 v40, v75
	v_mov_b32_e32 v35, v33
	v_pk_mov_b32 v[32:33], v[88:89], v[88:89] op_sel:[1,0]
	s_and_b64 vcc, exec, s[54:55]
	v_mov_b32_e32 v73, v33
	v_pk_mul_f32 v[38:39], v[72:73], v[34:35]
	v_pk_fma_f32 v[34:35], v[72:73], v[34:35], v[68:69]
	v_pk_mul_f32 v[38:39], v[68:69], v[38:39]
	v_mov_b32_e32 v33, v127
	v_mov_b32_e32 v34, v38
	v_pk_mul_f32 v[38:39], v[76:77], v[38:39]
	v_pk_fma_f32 v[34:35], v[76:77], v[34:35], v[70:71]
	v_pk_mul_f32 v[38:39], v[70:71], v[38:39]
	s_nop 0
	v_mov_b32_e32 v39, v35
	v_pk_mul_f32 v[34:35], v[92:93], v[38:39]
	v_pk_fma_f32 v[38:39], v[92:93], v[38:39], v[40:41]
	v_pk_mul_f32 v[34:35], v[74:75], v[34:35] op_sel:[1,0] op_sel_hi:[0,1]
	v_mov_b32_e32 v38, v34
	v_pk_mul_f32 v[34:35], v[88:89], v[34:35]
	v_pk_fma_f32 v[38:39], v[88:89], v[38:39], v[42:43]
	v_pk_mul_f32 v[34:35], v[76:77], v[34:35] op_sel:[1,0] op_sel_hi:[0,1]
	v_mov_b32_e32 v35, v39
	v_pk_mul_f32 v[38:39], v[90:91], v[34:35]
	v_pk_fma_f32 v[32:33], v[90:91], v[34:35], v[32:33]
	v_pk_mul_f32 v[38:39], v[88:89], v[38:39] op_sel:[1,0] op_sel_hi:[0,1]
	v_mov_b32_e32 v32, v38
	v_pk_mul_f32 v[34:35], v[84:85], v[38:39]
	v_pk_fma_f32 v[32:33], v[84:85], v[32:33], v[86:87]
	v_pk_mul_f32 v[34:35], v[84:85], v[34:35] op_sel:[1,0] op_sel_hi:[0,1]
	v_fma_f32 v32, 0, v134, v63
	v_mov_b32_e32 v35, v33
	v_fma_f32 v33, v133, v32, v62
	v_fma_f32 v33, v54, v33, v61
	v_fma_f32 v33, v82, v33, v60
	v_fma_f32 v33, v56, v33, v59
	v_fma_f32 v33, v80, v33, v58
	v_fma_f32 v33, v52, v33, v132
	v_fma_f32 v33, v78, v33, v130
	v_mul_f32_e32 v32, v134, v133
	v_fma_f32 v33, v98, v33, v129
	v_pk_mul_f32 v[38:39], v[54:55], v[32:33]
	v_pk_fma_f32 v[32:33], v[54:55], v[32:33], v[82:83]
	v_pk_mul_f32 v[38:39], v[82:83], v[38:39]
	v_add_u32_e32 v40, 0, v36
	v_mov_b32_e32 v39, v33
	v_pk_mov_b32 v[32:33], v[50:51], v[50:51] op_sel:[1,0]
	s_nop 0
	v_mov_b32_e32 v57, v33
	v_pk_mul_f32 v[136:137], v[56:57], v[38:39]
	v_pk_fma_f32 v[38:39], v[56:57], v[38:39], v[80:81]
	v_pk_mul_f32 v[136:137], v[80:81], v[136:137]
	v_mov_b32_e32 v33, v128
	v_mov_b32_e32 v38, v136
	v_pk_mul_f32 v[136:137], v[52:53], v[136:137]
	v_pk_fma_f32 v[38:39], v[52:53], v[38:39], v[78:79]
	v_pk_mul_f32 v[136:137], v[78:79], v[136:137]
	s_nop 0
	v_mov_b32_e32 v137, v39
	v_pk_mul_f32 v[38:39], v[98:99], v[136:137]
	v_pk_fma_f32 v[136:137], v[98:99], v[136:137], v[46:47]
	v_pk_mul_f32 v[38:39], v[54:55], v[38:39] op_sel:[1,0] op_sel_hi:[0,1]
	v_mov_b32_e32 v136, v38
	v_pk_mul_f32 v[38:39], v[50:51], v[38:39]
	v_pk_fma_f32 v[136:137], v[50:51], v[136:137], v[44:45]
	v_pk_mul_f32 v[38:39], v[52:53], v[38:39] op_sel:[1,0] op_sel_hi:[0,1]
	v_mov_b32_e32 v39, v137
	v_pk_mul_f32 v[136:137], v[96:97], v[38:39]
	v_pk_fma_f32 v[32:33], v[96:97], v[38:39], v[32:33]
	v_pk_mul_f32 v[136:137], v[50:51], v[136:137] op_sel:[1,0] op_sel_hi:[0,1]
	v_mov_b32_e32 v32, v136
	v_pk_mul_f32 v[38:39], v[48:49], v[136:137] op_sel:[1,0] op_sel_hi:[0,1]
	v_pk_mul_f32 v[38:39], v[48:49], v[38:39]
	v_pk_fma_f32 v[32:33], v[48:49], v[32:33], v[94:95] op_sel:[1,0,0] op_sel_hi:[0,1,1]
	v_mov_b32_e32 v39, v33
	ds_write2st64_b64 v37, v[34:35], v[38:39] offset1:8
	s_waitcnt lgkmcnt(0)
	s_barrier
	ds_read2st64_b64 v[34:37], v40 offset0:16 offset1:18
	s_waitcnt lgkmcnt(0)
	v_fma_f32 v32, 0, v34, v35
	v_fmac_f32_e32 v37, v32, v36
	ds_read2st64_b64 v[32:35], v40 offset0:20 offset1:22
	s_waitcnt lgkmcnt(0)
	v_fma_f32 v32, v37, v32, v33
	v_fmac_f32_e32 v35, v32, v34
	s_cbranch_vccnz .LBB0_674
	ds_read_b64 v[32:33], v40
	s_waitcnt lgkmcnt(0)
	v_fmac_f32_e32 v33, v35, v32
	v_mov_b32_e32 v35, v33
